# output-wave VALU trims: 2-op gather address, loss accumulated with packed fma
# speedup vs baseline: 1.0110x; 1.0110x over previous
.LBB0_81:
	ds_read_b128 v[194:197], v193 offset:4608
	ds_read_b128 v[198:201], v193 offset:4640
	ds_read_b128 v[202:205], v193 offset:4672
	ds_read_b128 v[206:209], v193 offset:4704
	s_min_u32 s6, s5, 11
	v_lshl_add_u32 v66, s6, 13, v191
	v_or_b32_e32 v66, v66, v178
	v_or_b32_e32 v67, 0x1000, v66
	global_load_dwordx4 v[174:177], v66, s[20:21] nt
	global_load_dwordx4 v[170:173], v67, s[20:21] nt
	s_add_i32 s0, s0, 2
	v_add_u32_e32 v192, 0x2400, v192
	v_add_u32_e32 v193, 0x2400, v193
	s_cmp_gt_u32 s5, 13
	s_waitcnt lgkmcnt(3)
	v_mfma_f32_32x32x16_f16 v[66:81], v[98:101], v[194:197], v[2:17]
	s_waitcnt lgkmcnt(2)
	v_mfma_f32_32x32x16_f16 v[66:81], v[102:105], v[198:201], v[66:81]
	s_waitcnt lgkmcnt(1)
	v_mfma_f32_32x32x16_f16 v[66:81], v[106:109], v[202:205], v[66:81]
	s_waitcnt lgkmcnt(0)
	v_mfma_f32_32x32x16_f16 v[66:81], v[110:113], v[206:209], v[66:81]
	v_mfma_f32_32x32x16_f16 v[82:97], v[114:117], v[194:197], v[18:33]
	s_nop 10
	v_and_b32_e32 v66, 0xffffffc0, v66
	v_and_or_b32 v67, v67, s1, 1
	v_and_or_b32 v68, v68, s1, 2
	v_and_or_b32 v69, v69, s1, 3
	v_med3_f32 v211, v66, v67, s4
	v_and_or_b32 v70, v70, s1, 4
	v_min3_f32 v210, v66, s4, v67
	v_and_or_b32 v71, v71, s1, 5
	v_mfma_f32_32x32x16_f16 v[82:97], v[118:121], v[198:201], v[82:97]
	v_med3_f32 v214, v210, v68, v69
	v_and_or_b32 v72, v72, s1, 6
	v_min3_f32 v212, v210, v68, v69
	v_and_or_b32 v73, v73, s1, 7
	v_min3_f32 v213, v211, s4, v214
	v_med3_f32 v211, v212, v70, v71
	v_and_or_b32 v74, v74, s1, 8
	v_min3_f32 v210, v212, v70, v71
	v_mfma_f32_32x32x16_f16 v[82:97], v[122:125], v[202:205], v[82:97]
	v_and_or_b32 v75, v75, s1, 9
	v_med3_f32 v214, v210, v72, v73
	v_and_or_b32 v76, v76, s1, 10
	v_min3_f32 v212, v210, v72, v73
	v_and_or_b32 v77, v77, s1, 11
	v_min3_f32 v213, v213, v211, v214
	v_med3_f32 v211, v212, v74, v75
	v_and_or_b32 v78, v78, s1, 12
	v_mfma_f32_32x32x16_f16 v[82:97], v[126:129], v[206:209], v[82:97]
	v_min3_f32 v210, v212, v74, v75
	v_and_or_b32 v79, v79, s1, 13
	v_med3_f32 v214, v210, v76, v77
	v_and_or_b32 v80, v80, s1, 14
	v_min3_f32 v212, v210, v76, v77
	v_and_or_b32 v81, v81, s1, 15
	v_min3_f32 v213, v213, v211, v214
	v_med3_f32 v211, v212, v78, v79
	v_min3_f32 v210, v212, v78, v79
	v_med3_f32 v214, v210, v80, v81
	v_min3_f32 v212, v210, v80, v81
	v_min3_f32 v213, v213, v211, v214
	v_mfma_f32_32x32x16_f16 v[66:81], v[130:133], v[194:197], v[34:49]
	v_and_or_b32 v82, v82, s1, 16
	v_and_or_b32 v83, v83, s1, 17
	v_and_or_b32 v84, v84, s1, 18
	v_and_or_b32 v85, v85, s1, 19
	v_med3_f32 v211, v212, v82, v83
	v_and_or_b32 v86, v86, s1, 20
	v_min3_f32 v210, v212, v82, v83
	v_and_or_b32 v87, v87, s1, 21
	v_mfma_f32_32x32x16_f16 v[66:81], v[134:137], v[198:201], v[66:81]
	v_med3_f32 v214, v210, v84, v85
	v_and_or_b32 v88, v88, s1, 22
	v_min3_f32 v212, v210, v84, v85
	v_and_or_b32 v89, v89, s1, 23
	v_min3_f32 v213, v213, v211, v214
	v_med3_f32 v211, v212, v86, v87
	v_and_or_b32 v90, v90, s1, 24
	v_min3_f32 v210, v212, v86, v87
	v_mfma_f32_32x32x16_f16 v[66:81], v[138:141], v[202:205], v[66:81]
	v_and_or_b32 v91, v91, s1, 25
	v_med3_f32 v214, v210, v88, v89
	v_and_or_b32 v92, v92, s1, 26
	v_min3_f32 v212, v210, v88, v89
	v_and_or_b32 v93, v93, s1, 27
	v_min3_f32 v213, v213, v211, v214
	v_med3_f32 v211, v212, v90, v91
	v_and_or_b32 v94, v94, s1, 28
	v_mfma_f32_32x32x16_f16 v[66:81], v[142:145], v[206:209], v[66:81]
	v_min3_f32 v210, v212, v90, v91
	v_and_or_b32 v95, v95, s1, 29
	v_med3_f32 v214, v210, v92, v93
	v_and_or_b32 v96, v96, s1, 30
	v_min3_f32 v212, v210, v92, v93
	v_and_or_b32 v97, v97, s1, 31
	v_min3_f32 v213, v213, v211, v214
	v_med3_f32 v211, v212, v94, v95
	v_min3_f32 v210, v212, v94, v95
	v_med3_f32 v214, v210, v96, v97
	v_min3_f32 v212, v210, v96, v97
	v_min3_f32 v213, v213, v211, v214
	v_mfma_f32_32x32x16_f16 v[82:97], v[146:149], v[194:197], v[50:65]
	v_and_or_b32 v66, v66, s1, 32
	v_and_or_b32 v67, v67, s1, 33
	v_and_or_b32 v68, v68, s1, 34
	v_and_or_b32 v69, v69, s1, 35
	v_med3_f32 v211, v212, v66, v67
	v_and_or_b32 v70, v70, s1, 36
	v_min3_f32 v210, v212, v66, v67
	v_and_or_b32 v71, v71, s1, 37
	v_mfma_f32_32x32x16_f16 v[82:97], v[150:153], v[198:201], v[82:97]
	v_med3_f32 v214, v210, v68, v69
	v_and_or_b32 v72, v72, s1, 38
	v_min3_f32 v212, v210, v68, v69
	v_and_or_b32 v73, v73, s1, 39
	v_min3_f32 v213, v213, v211, v214
	v_med3_f32 v211, v212, v70, v71
	v_and_or_b32 v74, v74, s1, 40
	v_min3_f32 v210, v212, v70, v71
	v_mfma_f32_32x32x16_f16 v[82:97], v[154:157], v[202:205], v[82:97]
	v_and_or_b32 v75, v75, s1, 41
	v_med3_f32 v214, v210, v72, v73
	v_and_or_b32 v76, v76, s1, 42
	v_min3_f32 v212, v210, v72, v73
	v_and_or_b32 v77, v77, s1, 43
	v_min3_f32 v213, v213, v211, v214
	v_med3_f32 v211, v212, v74, v75
	v_and_or_b32 v78, v78, s1, 44
	v_mfma_f32_32x32x16_f16 v[82:97], v[158:161], v[206:209], v[82:97]
	v_min3_f32 v210, v212, v74, v75
	v_and_or_b32 v79, v79, s1, 45
	v_med3_f32 v214, v210, v76, v77
	v_and_or_b32 v80, v80, s1, 46
	v_min3_f32 v212, v210, v76, v77
	v_and_or_b32 v81, v81, s1, 47
	v_min3_f32 v213, v213, v211, v214
	v_med3_f32 v211, v212, v78, v79
	v_min3_f32 v210, v212, v78, v79
	v_med3_f32 v214, v210, v80, v81
	v_min3_f32 v212, v210, v80, v81
	v_min3_f32 v213, v213, v211, v214
	v_and_or_b32 v82, v82, s1, 48
	v_and_or_b32 v83, v83, s1, 49
	v_and_or_b32 v84, v84, s1, 50
	v_and_or_b32 v85, v85, s1, 51
	v_med3_f32 v211, v212, v82, v83
	v_and_or_b32 v86, v86, s1, 52
	v_min3_f32 v210, v212, v82, v83
	v_and_or_b32 v87, v87, s1, 53
	v_med3_f32 v214, v210, v84, v85
	v_and_or_b32 v88, v88, s1, 54
	v_min3_f32 v212, v210, v84, v85
	v_and_or_b32 v89, v89, s1, 55
	v_min3_f32 v213, v213, v211, v214
	v_med3_f32 v211, v212, v86, v87
	v_and_or_b32 v90, v90, s1, 56
	v_min3_f32 v210, v212, v86, v87
	v_and_or_b32 v91, v91, s1, 57
	v_med3_f32 v214, v210, v88, v89
	v_and_or_b32 v92, v92, s1, 58
	v_min3_f32 v212, v210, v88, v89
	v_and_or_b32 v93, v93, s1, 59
	v_min3_f32 v213, v213, v211, v214
	v_med3_f32 v211, v212, v90, v91
	v_and_or_b32 v94, v94, s1, 60
	v_min3_f32 v210, v212, v90, v91
	v_and_or_b32 v95, v95, s1, 61
	v_med3_f32 v214, v210, v92, v93
	v_and_or_b32 v96, v96, s1, 62
	v_min3_f32 v212, v210, v92, v93
	v_or_b32_e32 v97, 63, v97
	v_min3_f32 v213, v213, v211, v214
	v_med3_f32 v211, v212, v94, v95
	v_min3_f32 v210, v212, v94, v95
	v_med3_f32 v214, v210, v96, v97
	v_min3_f32 v212, v210, v96, v97
	v_min3_f32 v213, v213, v211, v214
	ds_write_b64 v189, v[212:213] offset:4608
	s_waitcnt lgkmcnt(0)
	s_barrier
	s_cbranch_scc1 .LBB0_84
.LBB0_82:
	s_waitcnt vmcnt(3)
	v_cvt_pk_f16_f32 v67, v168, v169
	v_cvt_pk_f16_f32 v66, v166, v167
	ds_write_b64 v192, v[66:67]
	s_waitcnt vmcnt(2)
	v_cvt_pk_f16_f32 v67, v164, v165
	v_cvt_pk_f16_f32 v66, v162, v163
	ds_write_b64 v192, v[66:67] offset:2304
	ds_read_b128 v[194:197], v193
	ds_read_b128 v[198:201], v193 offset:32
	ds_read_b128 v[202:205], v193 offset:64
	ds_read_b128 v[206:209], v193 offset:96
	s_add_i32 s6, s0, -1
	s_add_i32 s5, s0, -2
	s_and_b32 s6, s6, 3
	s_min_u32 s7, s5, 12
	s_lshl_b32 s6, s6, 13
	v_lshl_add_u32 v66, s7, 13, v190
	s_add_i32 s6, s6, 0x12000
	v_or_b32_e32 v66, v66, v178
	v_lshl_or_b32 v67, v187, 4, s6
	v_lshl_or_b32 v84, v188, 4, s6
	v_or_b32_e32 v85, 0x1000, v66
	ds_write_b128 v67, v[166:169]
	ds_write_b128 v84, v[162:165]
	global_load_dwordx4 v[166:169], v66, s[20:21] nt
	global_load_dwordx4 v[162:165], v85, s[20:21] nt
	s_cmp_gt_u32 s5, 13
	s_waitcnt lgkmcnt(5)
	v_mfma_f32_32x32x16_f16 v[66:81], v[98:101], v[194:197], v[2:17]
	s_waitcnt lgkmcnt(4)
	v_mfma_f32_32x32x16_f16 v[66:81], v[102:105], v[198:201], v[66:81]
	s_waitcnt lgkmcnt(3)
	v_mfma_f32_32x32x16_f16 v[66:81], v[106:109], v[202:205], v[66:81]
	s_waitcnt lgkmcnt(2)
	v_mfma_f32_32x32x16_f16 v[66:81], v[110:113], v[206:209], v[66:81]
	v_mfma_f32_32x32x16_f16 v[82:97], v[114:117], v[194:197], v[18:33]
	s_nop 10
	v_and_b32_e32 v66, 0xffffffc0, v66
	v_and_or_b32 v67, v67, s1, 1
	v_and_or_b32 v68, v68, s1, 2
	v_and_or_b32 v69, v69, s1, 3
	v_med3_f32 v211, v66, v67, s4
	v_and_or_b32 v70, v70, s1, 4
	v_min3_f32 v210, v66, s4, v67
	v_and_or_b32 v71, v71, s1, 5
	v_mfma_f32_32x32x16_f16 v[82:97], v[118:121], v[198:201], v[82:97]
	v_med3_f32 v214, v210, v68, v69
	v_and_or_b32 v72, v72, s1, 6
	v_min3_f32 v212, v210, v68, v69
	v_and_or_b32 v73, v73, s1, 7
	v_min3_f32 v213, v211, s4, v214
	v_med3_f32 v211, v212, v70, v71
	v_and_or_b32 v74, v74, s1, 8
	v_min3_f32 v210, v212, v70, v71
	v_mfma_f32_32x32x16_f16 v[82:97], v[122:125], v[202:205], v[82:97]
	v_and_or_b32 v75, v75, s1, 9
	v_med3_f32 v214, v210, v72, v73
	v_and_or_b32 v76, v76, s1, 10
	v_min3_f32 v212, v210, v72, v73
	v_and_or_b32 v77, v77, s1, 11
	v_min3_f32 v213, v213, v211, v214
	v_med3_f32 v211, v212, v74, v75
	v_and_or_b32 v78, v78, s1, 12
	v_mfma_f32_32x32x16_f16 v[82:97], v[126:129], v[206:209], v[82:97]
	v_min3_f32 v210, v212, v74, v75
	v_and_or_b32 v79, v79, s1, 13
	v_med3_f32 v214, v210, v76, v77
	v_and_or_b32 v80, v80, s1, 14
	v_min3_f32 v212, v210, v76, v77
	v_and_or_b32 v81, v81, s1, 15
	v_min3_f32 v213, v213, v211, v214
	v_med3_f32 v211, v212, v78, v79
	v_min3_f32 v210, v212, v78, v79
	v_med3_f32 v214, v210, v80, v81
	v_min3_f32 v212, v210, v80, v81
	v_min3_f32 v213, v213, v211, v214
	v_mfma_f32_32x32x16_f16 v[66:81], v[130:133], v[194:197], v[34:49]
	v_and_or_b32 v82, v82, s1, 16
	v_and_or_b32 v83, v83, s1, 17
	v_and_or_b32 v84, v84, s1, 18
	v_and_or_b32 v85, v85, s1, 19
	v_med3_f32 v211, v212, v82, v83
	v_and_or_b32 v86, v86, s1, 20
	v_min3_f32 v210, v212, v82, v83
	v_and_or_b32 v87, v87, s1, 21
	v_mfma_f32_32x32x16_f16 v[66:81], v[134:137], v[198:201], v[66:81]
	v_med3_f32 v214, v210, v84, v85
	v_and_or_b32 v88, v88, s1, 22
	v_min3_f32 v212, v210, v84, v85
	v_and_or_b32 v89, v89, s1, 23
	v_min3_f32 v213, v213, v211, v214
	v_med3_f32 v211, v212, v86, v87
	v_and_or_b32 v90, v90, s1, 24
	v_min3_f32 v210, v212, v86, v87
	v_mfma_f32_32x32x16_f16 v[66:81], v[138:141], v[202:205], v[66:81]
	v_and_or_b32 v91, v91, s1, 25
	v_med3_f32 v214, v210, v88, v89
	v_and_or_b32 v92, v92, s1, 26
	v_min3_f32 v212, v210, v88, v89
	v_and_or_b32 v93, v93, s1, 27
	v_min3_f32 v213, v213, v211, v214
	v_med3_f32 v211, v212, v90, v91
	v_and_or_b32 v94, v94, s1, 28
	v_mfma_f32_32x32x16_f16 v[66:81], v[142:145], v[206:209], v[66:81]
	v_min3_f32 v210, v212, v90, v91
	v_and_or_b32 v95, v95, s1, 29
	v_med3_f32 v214, v210, v92, v93
	v_and_or_b32 v96, v96, s1, 30
	v_min3_f32 v212, v210, v92, v93
	v_and_or_b32 v97, v97, s1, 31
	v_min3_f32 v213, v213, v211, v214
	v_med3_f32 v211, v212, v94, v95
	v_min3_f32 v210, v212, v94, v95
	v_med3_f32 v214, v210, v96, v97
	v_min3_f32 v212, v210, v96, v97
	v_min3_f32 v213, v213, v211, v214
	v_mfma_f32_32x32x16_f16 v[82:97], v[146:149], v[194:197], v[50:65]
	v_and_or_b32 v66, v66, s1, 32
	v_and_or_b32 v67, v67, s1, 33
	v_and_or_b32 v68, v68, s1, 34
	v_and_or_b32 v69, v69, s1, 35
	v_med3_f32 v211, v212, v66, v67
	v_and_or_b32 v70, v70, s1, 36
	v_min3_f32 v210, v212, v66, v67
	v_and_or_b32 v71, v71, s1, 37
	v_mfma_f32_32x32x16_f16 v[82:97], v[150:153], v[198:201], v[82:97]
	v_med3_f32 v214, v210, v68, v69
	v_and_or_b32 v72, v72, s1, 38
	v_min3_f32 v212, v210, v68, v69
	v_and_or_b32 v73, v73, s1, 39
	v_min3_f32 v213, v213, v211, v214
	v_med3_f32 v211, v212, v70, v71
	v_and_or_b32 v74, v74, s1, 40
	v_min3_f32 v210, v212, v70, v71
	v_mfma_f32_32x32x16_f16 v[82:97], v[154:157], v[202:205], v[82:97]
	v_and_or_b32 v75, v75, s1, 41
	v_med3_f32 v214, v210, v72, v73
	v_and_or_b32 v76, v76, s1, 42
	v_min3_f32 v212, v210, v72, v73
	v_and_or_b32 v77, v77, s1, 43
	v_min3_f32 v213, v213, v211, v214
	v_med3_f32 v211, v212, v74, v75
	v_and_or_b32 v78, v78, s1, 44
	v_mfma_f32_32x32x16_f16 v[82:97], v[158:161], v[206:209], v[82:97]
	v_min3_f32 v210, v212, v74, v75
	v_and_or_b32 v79, v79, s1, 45
	v_med3_f32 v214, v210, v76, v77
	v_and_or_b32 v80, v80, s1, 46
	v_min3_f32 v212, v210, v76, v77
	v_and_or_b32 v81, v81, s1, 47
	v_min3_f32 v213, v213, v211, v214
	v_med3_f32 v211, v212, v78, v79
	v_min3_f32 v210, v212, v78, v79
	v_med3_f32 v214, v210, v80, v81
	v_min3_f32 v212, v210, v80, v81
	v_min3_f32 v213, v213, v211, v214
	v_and_or_b32 v82, v82, s1, 48
	v_and_or_b32 v83, v83, s1, 49
	v_and_or_b32 v84, v84, s1, 50
	v_and_or_b32 v85, v85, s1, 51
	v_med3_f32 v211, v212, v82, v83
	v_and_or_b32 v86, v86, s1, 52
	v_min3_f32 v210, v212, v82, v83
	v_and_or_b32 v87, v87, s1, 53
	v_med3_f32 v214, v210, v84, v85
	v_and_or_b32 v88, v88, s1, 54
	v_min3_f32 v212, v210, v84, v85
	v_and_or_b32 v89, v89, s1, 55
	v_min3_f32 v213, v213, v211, v214
	v_med3_f32 v211, v212, v86, v87
	v_and_or_b32 v90, v90, s1, 56
	v_min3_f32 v210, v212, v86, v87
	v_and_or_b32 v91, v91, s1, 57
	v_med3_f32 v214, v210, v88, v89
	v_and_or_b32 v92, v92, s1, 58
	v_min3_f32 v212, v210, v88, v89
	v_and_or_b32 v93, v93, s1, 59
	v_min3_f32 v213, v213, v211, v214
	v_med3_f32 v211, v212, v90, v91
	v_and_or_b32 v94, v94, s1, 60
	v_min3_f32 v210, v212, v90, v91
	v_and_or_b32 v95, v95, s1, 61
	v_med3_f32 v214, v210, v92, v93
	v_and_or_b32 v96, v96, s1, 62
	v_min3_f32 v212, v210, v92, v93
	v_or_b32_e32 v97, 63, v97
	v_min3_f32 v213, v213, v211, v214
	v_med3_f32 v211, v212, v94, v95
	v_min3_f32 v210, v212, v94, v95
	v_med3_f32 v214, v210, v96, v97
	v_min3_f32 v212, v210, v96, v97
	v_min3_f32 v213, v213, v211, v214
	ds_write_b64 v189, v[212:213]
	s_waitcnt lgkmcnt(0)
	s_barrier
	s_cbranch_scc1 .LBB0_81
	s_and_b32 s6, s0, 2
	s_waitcnt vmcnt(3)
	v_cvt_pk_f16_f32 v67, v176, v177
	v_cvt_pk_f16_f32 v66, v174, v175
	s_lshl_b32 s6, s6, 13
	ds_write_b64 v192, v[66:67] offset:4608
	s_waitcnt vmcnt(2)
	v_cvt_pk_f16_f32 v67, v172, v173
	v_cvt_pk_f16_f32 v66, v170, v171
	s_or_b32 s6, s6, 0x12000
	ds_write_b64 v192, v[66:67] offset:6912
	v_lshl_or_b32 v66, v187, 4, s6
	ds_write_b128 v66, v[174:177]
	v_lshl_or_b32 v66, v188, 4, s6
	ds_write_b128 v66, v[170:173]
	s_branch .LBB0_81

.LBB0_85:
	s_waitcnt vmcnt(3)
	v_mov_b32_e32 v167, 0
	s_and_b64 vcc, exec, s[0:1]
	s_cbranch_vccz .LBB0_107
	s_lshl_b32 s0, s33, 2
	s_and_b32 s0, s0, 12
	v_bfe_u32 v192, v0, 3, 2
	s_waitcnt vmcnt(0)
	v_or3_b32 v172, v192, s0, v182
	v_and_b32_e32 v170, 7, v0
	s_setprio 2
	v_mov_b32_e32 v222, 0
	v_mov_b32_e32 v223, 0
	ds_read_b128 v[162:165], v179
	ds_read_b128 v[166:169], v179 offset:32
	ds_read_b128 v[174:177], v179 offset:64
	ds_read_b128 v[188:191], v179 offset:96
	s_movk_i32 s16, 0xffc0
	s_mov_b32 s25, 0x7f61b1e6
	s_waitcnt lgkmcnt(0)
	v_mfma_f32_32x32x16_f16 v[66:81], v[98:101], v[162:165], v[2:17]
	s_lshl_b32 s1, s33, 4
	s_add_i32 s1, s1, 0x1a000
	s_mov_b32 s4, 0x1a000
	v_cmp_eq_u32_e32 vcc, 0, v170
	s_mov_b32 s17, 1
	v_add_u32_e32 v179, 0x1200, v179
	s_mov_b32 s26, 0x3db851ec
	v_mfma_f32_32x32x16_f16 v[66:81], v[102:105], v[166:169], v[66:81]
	s_movk_i32 s27, 0x3ff
	s_movk_i32 s28, 0x3ff0
	v_mfma_f32_32x32x16_f16 v[66:81], v[106:109], v[174:177], v[66:81]
	v_mfma_f32_32x32x16_f16 v[66:81], v[110:113], v[188:191], v[66:81]
	s_nop 11
	v_and_b32_e32 v82, 0xffffffc0, v66
	v_and_or_b32 v83, v67, s16, 1
	v_and_or_b32 v84, v68, s16, 2
	v_and_or_b32 v85, v69, s16, 3
	v_and_or_b32 v86, v70, s16, 4
	v_and_or_b32 v87, v71, s16, 5
	v_and_or_b32 v88, v72, s16, 6
	v_and_or_b32 v89, v73, s16, 7
	v_and_or_b32 v90, v74, s16, 8
	v_and_or_b32 v91, v75, s16, 9
	v_and_or_b32 v92, v76, s16, 10
	v_and_or_b32 v93, v77, s16, 11
	v_and_or_b32 v94, v78, s16, 12
	v_and_or_b32 v95, v79, s16, 13
	v_and_or_b32 v96, v80, s16, 14
	v_and_or_b32 v97, v81, s16, 15
	v_mfma_f32_32x32x16_f16 v[66:81], v[114:117], v[162:165], v[18:33]
	v_med3_f32 v171, v82, v83, s25
	v_min3_f32 v82, v82, s25, v83
	v_med3_f32 v83, v82, v84, v85
	v_min3_f32 v82, v82, v84, v85
	v_med3_f32 v84, v82, v86, v87
	v_min3_f32 v82, v82, v86, v87
	v_min3_f32 v83, v171, s25, v83
	v_mfma_f32_32x32x16_f16 v[66:81], v[118:121], v[166:169], v[66:81]
	v_med3_f32 v85, v82, v88, v89
	v_min3_f32 v82, v82, v88, v89
	v_min3_f32 v83, v83, v84, v85
	v_med3_f32 v84, v82, v90, v91
	v_min3_f32 v82, v82, v90, v91
	v_med3_f32 v85, v82, v92, v93
	v_min3_f32 v82, v82, v92, v93
	v_mfma_f32_32x32x16_f16 v[66:81], v[122:125], v[174:177], v[66:81]
	v_min3_f32 v83, v83, v84, v85
	v_med3_f32 v84, v82, v94, v95
	v_min3_f32 v82, v82, v94, v95
	v_med3_f32 v85, v82, v96, v97
	v_min3_f32 v171, v82, v96, v97
	v_min3_f32 v173, v83, v84, v85
	v_mfma_f32_32x32x16_f16 v[66:81], v[126:129], v[188:191], v[66:81]
	v_mfma_f32_32x32x16_f16 v[82:97], v[130:133], v[162:165], v[34:49]
	s_nop 10
	v_and_or_b32 v66, v66, s16, 16
	v_and_or_b32 v67, v67, s16, 17
	v_and_or_b32 v68, v68, s16, 18
	v_and_or_b32 v69, v69, s16, 19
	v_med3_f32 v187, v171, v66, v67
	v_min3_f32 v66, v171, v66, v67
	v_and_or_b32 v70, v70, s16, 20
	v_and_or_b32 v71, v71, s16, 21
	v_med3_f32 v67, v66, v68, v69
	v_min3_f32 v66, v66, v68, v69
	v_and_or_b32 v72, v72, s16, 22
	v_and_or_b32 v73, v73, s16, 23
	v_med3_f32 v68, v66, v70, v71
	v_min3_f32 v66, v66, v70, v71
	v_and_or_b32 v74, v74, s16, 24
	v_and_or_b32 v75, v75, s16, 25
	v_min3_f32 v67, v173, v187, v67
	v_med3_f32 v69, v66, v72, v73
	v_min3_f32 v66, v66, v72, v73
	v_and_or_b32 v76, v76, s16, 26
	v_and_or_b32 v77, v77, s16, 27
	v_min3_f32 v67, v67, v68, v69
	v_med3_f32 v68, v66, v74, v75
	v_min3_f32 v66, v66, v74, v75
	v_and_or_b32 v78, v78, s16, 28
	v_and_or_b32 v79, v79, s16, 29
	v_med3_f32 v69, v66, v76, v77
	v_min3_f32 v66, v66, v76, v77
	v_and_or_b32 v80, v80, s16, 30
	v_and_or_b32 v81, v81, s16, 31
	v_min3_f32 v67, v67, v68, v69
	v_med3_f32 v68, v66, v78, v79
	v_min3_f32 v66, v66, v78, v79
	v_med3_f32 v69, v66, v80, v81
	v_mfma_f32_32x32x16_f16 v[82:97], v[134:137], v[166:169], v[82:97]
	v_min3_f32 v171, v66, v80, v81
	v_min3_f32 v173, v67, v68, v69
	v_mfma_f32_32x32x16_f16 v[66:81], v[146:149], v[162:165], v[50:65]
	v_mfma_f32_32x32x16_f16 v[82:97], v[138:141], v[174:177], v[82:97]
	v_mfma_f32_32x32x16_f16 v[66:81], v[150:153], v[166:169], v[66:81]
	v_mov_b32_e32 v167, 0
	v_mfma_f32_32x32x16_f16 v[82:97], v[142:145], v[188:191], v[82:97]
	v_mfma_f32_32x32x16_f16 v[66:81], v[154:157], v[174:177], v[66:81]
	s_nop 10
	v_and_or_b32 v82, v82, s16, 32
	v_and_or_b32 v83, v83, s16, 33
	v_and_or_b32 v84, v84, s16, 34
	v_and_or_b32 v85, v85, s16, 35
	v_med3_f32 v162, v171, v82, v83
	v_min3_f32 v82, v171, v82, v83
	v_and_or_b32 v86, v86, s16, 36
	v_mfma_f32_32x32x16_f16 v[66:81], v[158:161], v[188:191], v[66:81]
	v_and_or_b32 v87, v87, s16, 37
	v_med3_f32 v83, v82, v84, v85
	v_min3_f32 v82, v82, v84, v85
	v_and_or_b32 v88, v88, s16, 38
	v_and_or_b32 v89, v89, s16, 39
	v_med3_f32 v84, v82, v86, v87
	v_min3_f32 v82, v82, v86, v87
	v_and_or_b32 v90, v90, s16, 40
	v_and_or_b32 v91, v91, s16, 41
	v_min3_f32 v83, v173, v162, v83
	v_med3_f32 v85, v82, v88, v89
	v_min3_f32 v82, v82, v88, v89
	v_and_or_b32 v92, v92, s16, 42
	v_and_or_b32 v93, v93, s16, 43
	v_min3_f32 v83, v83, v84, v85
	v_med3_f32 v84, v82, v90, v91
	v_min3_f32 v82, v82, v90, v91
	v_and_or_b32 v94, v94, s16, 44
	v_and_or_b32 v95, v95, s16, 45
	v_med3_f32 v85, v82, v92, v93
	v_min3_f32 v82, v82, v92, v93
	v_and_or_b32 v96, v96, s16, 46
	v_and_or_b32 v97, v97, s16, 47
	v_min3_f32 v83, v83, v84, v85
	v_med3_f32 v84, v82, v94, v95
	v_min3_f32 v82, v82, v94, v95
	v_med3_f32 v85, v82, v96, v97
	v_min3_f32 v82, v82, v96, v97
	v_and_or_b32 v66, v66, s16, 48
	v_and_or_b32 v67, v67, s16, 49
	v_min3_f32 v83, v83, v84, v85
	v_and_or_b32 v68, v68, s16, 50
	v_and_or_b32 v69, v69, s16, 51
	v_med3_f32 v84, v82, v66, v67
	v_min3_f32 v66, v82, v66, v67
	v_and_or_b32 v70, v70, s16, 52
	v_and_or_b32 v71, v71, s16, 53
	v_med3_f32 v67, v66, v68, v69
	v_min3_f32 v66, v66, v68, v69
	v_and_or_b32 v72, v72, s16, 54
	v_and_or_b32 v73, v73, s16, 55
	v_med3_f32 v68, v66, v70, v71
	v_min3_f32 v66, v66, v70, v71
	v_and_or_b32 v74, v74, s16, 56
	v_and_or_b32 v75, v75, s16, 57
	v_min3_f32 v67, v83, v84, v67
	v_med3_f32 v69, v66, v72, v73
	v_min3_f32 v66, v66, v72, v73
	v_and_or_b32 v76, v76, s16, 58
	v_and_or_b32 v77, v77, s16, 59
	v_min3_f32 v67, v67, v68, v69
	v_med3_f32 v68, v66, v74, v75
	v_min3_f32 v66, v66, v74, v75
	v_and_or_b32 v78, v78, s16, 60
	v_and_or_b32 v79, v79, s16, 61
	v_med3_f32 v69, v66, v76, v77
	v_min3_f32 v66, v66, v76, v77
	v_and_or_b32 v80, v80, s16, 62
	v_or_b32_e32 v81, 63, v81
	v_min3_f32 v67, v67, v68, v69
	v_med3_f32 v68, v66, v78, v79
	v_min3_f32 v66, v66, v78, v79
	v_med3_f32 v69, v66, v80, v81
	v_min3_f32 v67, v67, v68, v69
	v_lshlrev_b32_e32 v68, 3, v184
	v_min3_f32 v66, v66, v80, v81
	v_add3_u32 v177, s1, v185, v68
	ds_write_b64 v177, v[66:67]
	v_mul_u32_u24_e32 v66, 0x90, v172
	v_lshlrev_b32_e32 v67, 4, v170
	v_add3_u32 v185, v67, v66, s4
	v_and_b32_e32 v66, 0xff, v0
	v_mov_b32_e32 v67, 0x12000
	v_or_b32_e32 v173, 16, v183
	s_mov_b32 s1, 0x12000
	v_lshl_or_b32 v175, v66, 4, v67
	v_lshlrev_b32_e32 v66, 8, v173
	v_or3_b32 v174, v66, v178, s1
	s_lshl_b32 s1, s2, 17
	v_or3_b32 v166, s1, v186, v178
	s_waitcnt lgkmcnt(0)
	s_barrier
	v_lshl_add_u64 v[168:169], s[12:13], 0, v[166:167]
	v_or_b32_e32 v166, 0x1000, v166
	v_lshlrev_b32_e32 v176, 7, v170
	v_lshl_add_u64 v[170:171], s[12:13], 0, v[166:167]
	v_add3_u32 v166, v182, s0, v192
	v_mov_b32_e32 v66, 0x20c00
	v_or_b32_e32 v187, 4, v176
	v_lshlrev_b32_e32 v188, 2, v183
	v_lshl_or_b32 v186, v166, 2, v66
	v_mov_b32_e32 v189, 0x21d44
	s_mov_b64 s[4:5], 0x2000
	v_bfrev_b32_e32 v190, 1
	s_branch .LBB0_88

.LBB0_88:
	s_add_i32 s29, s17, -1
	s_and_b32 s0, s29, 1
	s_mulk_i32 s0, 0x1200
	v_add_u32_e32 v254, s0, v185
	ds_read_b128 v[250:253], v254
	s_add_i32 s1, s17, -2
	s_and_b32 s1, s1, 3
	v_lshl_add_u32 v66, s1, 13, v175
	v_lshl_add_u32 v67, s1, 13, v174
	ds_read_b128 v[82:85], v66
	ds_read_b128 v[86:89], v67
	ds_read_b128 v[194:197], v179
	ds_read_b128 v[198:201], v179 offset:32
	ds_read_b128 v[202:205], v179 offset:64
	ds_read_b128 v[206:209], v179 offset:96
	s_cmp_lt_u32 s17, 2
	s_cbranch_scc1 .Low_noout
	v_cmp_lt_i32_e64 s[0:1], -1, v192
	s_waitcnt vmcnt(0) lgkmcnt(4)
	s_and_saveexec_b64 s[6:7], s[0:1]
	s_cbranch_execz .Low_a_donel
	v_pk_add_f32 v[66:67], v[246:247], v[82:83] neg_lo:[0,1] neg_hi:[0,1]
	v_pk_add_f32 v[74:75], v[248:249], v[84:85] neg_lo:[0,1] neg_hi:[0,1]
	v_pk_fma_f32 v[222:223], v[66:67], v[66:67], v[222:223]
	v_pk_fma_f32 v[222:223], v[74:75], v[74:75], v[222:223]
	v_pk_add_f32 v[66:67], v[82:83], v[66:67]
	v_pk_add_f32 v[68:69], v[84:85], v[74:75]
	global_store_dwordx4 v[168:169], v[66:69], off sc0 sc1
	s_nop 1
.Low_a_donel:
	s_or_b64 exec, exec, s[6:7]
	v_cmp_lt_i32_e64 s[0:1], -1, v191
	s_and_saveexec_b64 s[6:7], s[0:1]
	s_cbranch_execz .Low_b_donel
	v_pk_add_f32 v[70:71], v[162:163], v[86:87] neg_lo:[0,1] neg_hi:[0,1]
	v_pk_add_f32 v[72:73], v[164:165], v[88:89] neg_lo:[0,1] neg_hi:[0,1]
	v_pk_fma_f32 v[222:223], v[70:71], v[70:71], v[222:223]
	v_pk_fma_f32 v[222:223], v[72:73], v[72:73], v[222:223]
	v_pk_add_f32 v[66:67], v[86:87], v[70:71]
	v_pk_add_f32 v[68:69], v[88:89], v[72:73]
	global_store_dwordx4 v[170:171], v[66:69], off sc0 sc1
	s_nop 1

.Low_m_done:
	s_or_b64 exec, exec, s[6:7]
	s_waitcnt lgkmcnt(0)
	v_mfma_f32_32x32x16_f16 v[66:81], v[98:101], v[194:197], v[2:17]
	v_mfma_f32_32x32x16_f16 v[66:81], v[102:105], v[198:201], v[66:81]
	v_add_u32_e32 v254, 0x20c00, v188
	s_waitcnt lgkmcnt(0)
	ds_read_b32 v191, v254 offset:64
	ds_read_b32 v192, v254
	v_mfma_f32_32x32x16_f16 v[66:81], v[106:109], v[202:205], v[66:81]
	v_mfma_f32_32x32x16_f16 v[66:81], v[110:113], v[206:209], v[66:81]
	v_mfma_f32_32x32x16_f16 v[82:97], v[114:117], v[194:197], v[18:33]
	s_waitcnt lgkmcnt(0)
	v_and_b32_e32 v212, s27, v191
	v_lshl_or_b32 v212, v212, 8, v178
	global_load_dwordx4 v[162:165], v212, s[22:23]
	v_and_b32_e32 v213, s27, v192
	v_lshl_or_b32 v213, v213, 8, v178
	global_load_dwordx4 v[246:249], v213, s[22:23]
	s_nop 3
	v_and_b32_e32 v66, 0xffffffc0, v66
	v_and_or_b32 v67, v67, s16, 1
	v_and_or_b32 v68, v68, s16, 2
	v_and_or_b32 v69, v69, s16, 3
	v_med3_f32 v211, v66, v67, s25
	v_and_or_b32 v70, v70, s16, 4
	v_min3_f32 v210, v66, s25, v67
	v_and_or_b32 v71, v71, s16, 5
	v_mfma_f32_32x32x16_f16 v[82:97], v[118:121], v[198:201], v[82:97]
	v_med3_f32 v214, v210, v68, v69
	v_and_or_b32 v72, v72, s16, 6
	v_min3_f32 v212, v210, v68, v69
	v_and_or_b32 v73, v73, s16, 7
	v_min3_f32 v213, v211, s25, v214
	v_med3_f32 v211, v212, v70, v71
	v_and_or_b32 v74, v74, s16, 8
	v_min3_f32 v210, v212, v70, v71
	v_mfma_f32_32x32x16_f16 v[82:97], v[122:125], v[202:205], v[82:97]
	v_and_or_b32 v75, v75, s16, 9
	v_med3_f32 v214, v210, v72, v73
	v_and_or_b32 v76, v76, s16, 10
	v_min3_f32 v212, v210, v72, v73
	v_and_or_b32 v77, v77, s16, 11
	v_min3_f32 v213, v213, v211, v214
	v_med3_f32 v211, v212, v74, v75
	v_and_or_b32 v78, v78, s16, 12
	v_mfma_f32_32x32x16_f16 v[82:97], v[126:129], v[206:209], v[82:97]
	v_min3_f32 v210, v212, v74, v75
	v_and_or_b32 v79, v79, s16, 13
	v_med3_f32 v214, v210, v76, v77
	v_and_or_b32 v80, v80, s16, 14
	v_min3_f32 v212, v210, v76, v77
	v_and_or_b32 v81, v81, s16, 15
	v_min3_f32 v213, v213, v211, v214
	v_med3_f32 v211, v212, v78, v79
	v_min3_f32 v210, v212, v78, v79
	v_med3_f32 v214, v210, v80, v81
	v_min3_f32 v212, v210, v80, v81
	v_min3_f32 v213, v213, v211, v214
	v_mfma_f32_32x32x16_f16 v[66:81], v[130:133], v[194:197], v[34:49]
	v_and_or_b32 v82, v82, s16, 16
	v_and_or_b32 v83, v83, s16, 17
	v_and_or_b32 v84, v84, s16, 18
	v_and_or_b32 v85, v85, s16, 19
	v_med3_f32 v211, v212, v82, v83
	v_and_or_b32 v86, v86, s16, 20
	v_min3_f32 v210, v212, v82, v83
	v_and_or_b32 v87, v87, s16, 21
	v_mfma_f32_32x32x16_f16 v[66:81], v[134:137], v[198:201], v[66:81]
	v_med3_f32 v214, v210, v84, v85
	v_and_or_b32 v88, v88, s16, 22
	v_min3_f32 v212, v210, v84, v85
	v_and_or_b32 v89, v89, s16, 23
	v_min3_f32 v213, v213, v211, v214
	v_med3_f32 v211, v212, v86, v87
	v_and_or_b32 v90, v90, s16, 24
	v_min3_f32 v210, v212, v86, v87
	v_mfma_f32_32x32x16_f16 v[66:81], v[138:141], v[202:205], v[66:81]
	v_and_or_b32 v91, v91, s16, 25
	v_med3_f32 v214, v210, v88, v89
	v_and_or_b32 v92, v92, s16, 26
	v_min3_f32 v212, v210, v88, v89
	v_and_or_b32 v93, v93, s16, 27
	v_min3_f32 v213, v213, v211, v214
	v_med3_f32 v211, v212, v90, v91
	v_and_or_b32 v94, v94, s16, 28
	v_mfma_f32_32x32x16_f16 v[66:81], v[142:145], v[206:209], v[66:81]
	v_min3_f32 v210, v212, v90, v91
	v_and_or_b32 v95, v95, s16, 29
	v_med3_f32 v214, v210, v92, v93
	v_and_or_b32 v96, v96, s16, 30
	v_min3_f32 v212, v210, v92, v93
	v_and_or_b32 v97, v97, s16, 31
	v_min3_f32 v213, v213, v211, v214
	v_med3_f32 v211, v212, v94, v95
	v_min3_f32 v210, v212, v94, v95
	v_med3_f32 v214, v210, v96, v97
	v_min3_f32 v212, v210, v96, v97
	v_min3_f32 v213, v213, v211, v214
	v_mfma_f32_32x32x16_f16 v[82:97], v[146:149], v[194:197], v[50:65]
	v_and_or_b32 v66, v66, s16, 32
	v_and_or_b32 v67, v67, s16, 33
	v_and_or_b32 v68, v68, s16, 34
	v_and_or_b32 v69, v69, s16, 35
	v_med3_f32 v211, v212, v66, v67
	v_and_or_b32 v70, v70, s16, 36
	v_min3_f32 v210, v212, v66, v67
	v_and_or_b32 v71, v71, s16, 37
	v_mfma_f32_32x32x16_f16 v[82:97], v[150:153], v[198:201], v[82:97]
	v_med3_f32 v214, v210, v68, v69
	v_and_or_b32 v72, v72, s16, 38
	v_min3_f32 v212, v210, v68, v69
	v_and_or_b32 v73, v73, s16, 39
	v_min3_f32 v213, v213, v211, v214
	v_med3_f32 v211, v212, v70, v71
	v_and_or_b32 v74, v74, s16, 40
	v_min3_f32 v210, v212, v70, v71
	v_mfma_f32_32x32x16_f16 v[82:97], v[154:157], v[202:205], v[82:97]
	v_and_or_b32 v75, v75, s16, 41
	v_med3_f32 v214, v210, v72, v73
	v_and_or_b32 v76, v76, s16, 42
	v_min3_f32 v212, v210, v72, v73
	v_and_or_b32 v77, v77, s16, 43
	v_min3_f32 v213, v213, v211, v214
	v_med3_f32 v211, v212, v74, v75
	v_and_or_b32 v78, v78, s16, 44
	v_mfma_f32_32x32x16_f16 v[82:97], v[158:161], v[206:209], v[82:97]
	v_min3_f32 v210, v212, v74, v75
	v_and_or_b32 v79, v79, s16, 45
	v_med3_f32 v214, v210, v76, v77
	v_and_or_b32 v80, v80, s16, 46
	v_min3_f32 v212, v210, v76, v77
	v_and_or_b32 v81, v81, s16, 47
	v_min3_f32 v213, v213, v211, v214
	v_med3_f32 v211, v212, v78, v79
	v_min3_f32 v210, v212, v78, v79
	v_med3_f32 v214, v210, v80, v81
	v_min3_f32 v212, v210, v80, v81
	v_min3_f32 v213, v213, v211, v214
	v_and_or_b32 v82, v82, s16, 48
	v_and_or_b32 v83, v83, s16, 49
	v_and_or_b32 v84, v84, s16, 50
	v_and_or_b32 v85, v85, s16, 51
	v_med3_f32 v211, v212, v82, v83
	v_and_or_b32 v86, v86, s16, 52
	v_min3_f32 v210, v212, v82, v83
	v_and_or_b32 v87, v87, s16, 53
	v_med3_f32 v214, v210, v84, v85
	v_and_or_b32 v88, v88, s16, 54
	v_min3_f32 v212, v210, v84, v85
	v_and_or_b32 v89, v89, s16, 55
	v_min3_f32 v213, v213, v211, v214
	v_med3_f32 v211, v212, v86, v87
	v_and_or_b32 v90, v90, s16, 56
	v_min3_f32 v210, v212, v86, v87
	v_and_or_b32 v91, v91, s16, 57
	v_med3_f32 v214, v210, v88, v89
	v_and_or_b32 v92, v92, s16, 58
	v_min3_f32 v212, v210, v88, v89
	v_and_or_b32 v93, v93, s16, 59
	v_min3_f32 v213, v213, v211, v214
	v_med3_f32 v211, v212, v90, v91
	v_and_or_b32 v94, v94, s16, 60
	v_min3_f32 v210, v212, v90, v91
	v_and_or_b32 v95, v95, s16, 61
	v_med3_f32 v214, v210, v92, v93
	v_and_or_b32 v96, v96, s16, 62
	v_min3_f32 v212, v210, v92, v93
	v_or_b32_e32 v97, 63, v97
	v_min3_f32 v213, v213, v211, v214
	v_med3_f32 v211, v212, v94, v95
	v_min3_f32 v210, v212, v94, v95
	v_med3_f32 v214, v210, v96, v97
	v_min3_f32 v212, v210, v96, v97
	v_min3_f32 v213, v213, v211, v214
	s_and_b32 s0, s17, 1
	s_mulk_i32 s0, 0x1200
	v_add_u32_e32 v254, s0, v177
	ds_write_b64 v254, v[212:213]
	s_branch .LBB0_87
.LBB0_97:
	s_add_i32 s1, s17, -2
	s_and_b32 s1, s1, 3
	v_lshl_add_u32 v66, s1, 13, v175
	v_lshl_add_u32 v67, s1, 13, v174
	ds_read_b128 v[82:85], v66
	ds_read_b128 v[86:89], v67
	v_cmp_lt_i32_e64 s[0:1], -1, v192
	s_waitcnt vmcnt(0) lgkmcnt(0)
	s_and_saveexec_b64 s[6:7], s[0:1]
	s_cbranch_execz .Low_a_doned
	v_pk_add_f32 v[66:67], v[246:247], v[82:83] neg_lo:[0,1] neg_hi:[0,1]
	v_pk_add_f32 v[74:75], v[248:249], v[84:85] neg_lo:[0,1] neg_hi:[0,1]
	v_pk_fma_f32 v[222:223], v[66:67], v[66:67], v[222:223]
	v_pk_fma_f32 v[222:223], v[74:75], v[74:75], v[222:223]
	v_pk_add_f32 v[66:67], v[82:83], v[66:67]
	v_pk_add_f32 v[68:69], v[84:85], v[74:75]
	global_store_dwordx4 v[168:169], v[66:69], off sc0 sc1
	s_nop 1

.Low_b_doned:
	s_or_b64 exec, exec, s[6:7]
	v_add_f32_e32 v167, v167, v222
	v_add_f32_e32 v167, v167, v223
	ds_read_b128 v[66:69], v185 offset:4608
	s_movk_i32 s0, 0xfc03
	s_waitcnt lgkmcnt(0)
	v_lshlrev_b32_e32 v71, 1, v68
	v_lshlrev_b32_e32 v70, 1, v66
	v_and_b32_e32 v71, 0x78, v71
	v_and_b32_e32 v66, 0xfffffc03, v66
	v_and_b32_e32 v70, 0x78, v70
	v_and_or_b32 v68, v68, s0, v71
	v_or3_b32 v66, v66, v70, v176
	v_or3_b32 v68, v68, v176, 4
	v_max_f32_e32 v66, v66, v66
	v_max_f32_e32 v68, v68, v68
	v_min_f32_e32 v70, v66, v68
	v_max_f32_e32 v66, v66, v68
	v_mov_b32_e32 v68, 0
	v_min3_f32 v66, v67, v69, v66
	v_mov_b32_e32 v69, 0
	v_mov_b32_dpp v68, v70 quad_perm:[1,0,3,2] row_mask:0xf bank_mask:0xf
	v_max_f32_e32 v68, v68, v68
	v_mov_b32_dpp v69, v66 quad_perm:[1,0,3,2] row_mask:0xf bank_mask:0xf
	v_max_f32_e32 v71, v70, v68
	v_min3_f32 v66, v66, v69, v71
	v_min_f32_e32 v69, v70, v68
	v_mov_b32_e32 v68, 0
	v_mov_b32_e32 v70, 0
	v_mov_b32_e32 v67, 0
	v_mov_b32_dpp v68, v69 quad_perm:[2,3,0,1] row_mask:0xf bank_mask:0xf
	v_max_f32_e32 v71, v68, v68
	v_mov_b32_dpp v70, v66 quad_perm:[2,3,0,1] row_mask:0xf bank_mask:0xf
	v_max_f32_e32 v68, v69, v71
	v_min3_f32 v68, v66, v70, v68
	v_min_f32_e32 v66, v69, v71
	v_mov_b32_e32 v69, 0
	v_mov_b32_dpp v67, v68 row_half_mirror row_mask:0xf bank_mask:0xf
	s_nop 0
	v_mov_b32_dpp v69, v66 row_half_mirror row_mask:0xf bank_mask:0xf
	s_and_saveexec_b64 s[0:1], vcc
	s_cbranch_execz .LBB0_102
	v_max_f32_e32 v69, v69, v69
	v_max_f32_e32 v70, v66, v66
	v_min_f32_e32 v66, v70, v69
	v_max_f32_e32 v69, v70, v69
	v_min3_f32 v67, v68, v67, v69
	v_sub_f32_e32 v67, v67, v66
	s_mov_b32 s4, 0x3db851ec
	v_bfrev_b32_e32 v68, 1
	v_cmp_gt_f32_e32 vcc, s4, v67
	s_movk_i32 s4, 0x3ff
	s_nop 0
	v_cndmask_b32_e32 v67, 0, v68, vcc
	v_mov_b32_e32 v68, 0x21380
	v_and_or_b32 v67, v66, s4, v67
	v_lshl_or_b32 v68, v172, 2, v68
	ds_write_b32 v68, v67
	s_and_b64 exec, exec, vcc
	s_cbranch_execz .LBB0_102
	s_mov_b64 s[6:7], exec
	v_mbcnt_lo_u32_b32 v67, s6, 0
	v_mbcnt_hi_u32_b32 v67, s7, v67
	v_cmp_eq_u32_e32 vcc, 0, v67
	s_and_saveexec_b64 s[4:5], vcc
	s_bcnt1_i32_b64 s6, s[6:7]
	v_mov_b32_e32 v68, 0x21d44
	v_mov_b32_e32 v69, s6
	ds_add_rtn_u32 v68, v68, v69
	s_or_b64 exec, exec, s[4:5]
	s_waitcnt lgkmcnt(0)
	v_readfirstlane_b32 s4, v68
	v_or_b32_e32 v69, 0x1e0, v172
	v_add_f32_e32 v66, 0x3dcccccd, v66
	v_add_lshl_u32 v67, s4, v67, 2
	v_add_u32_e32 v68, 0x21400, v67
	v_add_u32_e32 v67, 0x20400, v67
	ds_write_b32 v68, v69
	ds_write_b32 v67, v66
